# baseline (speedup 1.0000x reference)
_Z9l1_kernelPKiS0_P15HIP_vector_typeIjLj2EEPiS4_PKfS6_S6_S6_PfP6__half:
	s_cmp_gt_u32 s2, 42
	s_mov_b64 s[4:5], -1
	s_cbranch_scc0 .LBB0_17
	s_mul_i32 s15, s2, 0xeb
	s_add_i32 s3, s15, 0xffffd887
	s_min_i32 s16, s3, 0xc265
	s_add_i32 s12, s16, 0xeb
	s_cmp_ge_i32 s3, s12
	s_cbranch_scc1 .LBB0_16
	s_load_dwordx4 s[4:7], s[0:1], 0x28
	s_load_dwordx2 s[10:11], s[0:1], 0x38
	s_load_dwordx4 s[24:27], s[0:1], 0x40
	s_load_dwordx2 s[28:29], s[0:1], 0x50
	v_lshlrev_b32_e32 v1, 4, v0
	v_and_b32_e32 v2, 0x1f0, v1
	v_mov_b32_e32 v3, 0
	v_lshrrev_b32_e32 v1, 5, v0
	s_add_i32 s13, s16, 0xea
	s_waitcnt lgkmcnt(0)
	v_lshl_add_u64 v[110:111], s[4:5], 0, v[2:3]
	v_add_u32_e32 v2, s3, v1
	v_min_i32_e32 v2, s13, v2
	v_ashrrev_i32_e32 v3, 31, v2
	v_lshlrev_b64 v[2:3], 9, v[2:3]
	v_lshl_add_u64 v[10:11], v[110:111], 0, v[2:3]
	v_or_b32_e32 v2, 0x200, v0
	v_lshrrev_b32_e32 v146, 5, v2
	v_add_u32_e32 v2, s3, v146
	v_min_i32_e32 v2, s13, v2
	v_ashrrev_i32_e32 v3, 31, v2
	v_lshlrev_b64 v[2:3], 9, v[2:3]
	v_or_b32_e32 v147, 32, v1
	v_lshl_add_u64 v[12:13], v[110:111], 0, v[2:3]
	global_load_dwordx4 v[2:5], v[10:11], off
	global_load_dwordx4 v[6:9], v[12:13], off
	v_add_u32_e32 v10, s3, v147
	v_min_i32_e32 v10, s13, v10
	v_ashrrev_i32_e32 v11, 31, v10
	v_lshlrev_b64 v[10:11], 9, v[10:11]
	v_lshl_add_u64 v[10:11], v[110:111], 0, v[10:11]
	global_load_dwordx4 v[10:13], v[10:11], off
	v_lshrrev_b32_e32 v149, 6, v0
	s_movk_i32 s4, 0x200
	v_and_b32_e32 v150, 15, v0
	v_cmp_gt_u32_e32 vcc, s4, v0
	v_lshlrev_b32_e32 v151, 4, v149
	s_and_saveexec_b64 s[4:5], vcc
	s_xor_b64 s[4:5], exec, s[4:5]
	v_or_b32_e32 v32, v151, v150
	s_or_saveexec_b64 s[4:5], s[4:5]
	v_lshlrev_b32_e32 v14, 1, v150
	v_mov_b64_e32 v[30:31], s[6:7]
	s_xor_b64 exec, exec, s[4:5]
	v_and_b32_e32 v15, 0x60, v151
	v_bfe_u32 v16, v0, 6, 1
	v_or3_b32 v32, v16, v15, v14
	v_mov_b64_e32 v[30:31], s[10:11]
	s_or_b64 exec, exec, s[4:5]
	s_movk_i32 s17, 0x110
	s_mov_b32 s14, 0x7060302
	s_sub_i32 s19, s16, s3
	s_addk_i32 s19, 0x11a
	v_readfirstlane_b32 s30, v149
	v_bfe_u32 v152, v0, 4, 2
	v_lshlrev_b32_e32 v153, 5, v149
	v_and_b32_e32 v153, 0x60, v153
	v_or_b32_e32 v144, v151, v150
	v_lshlrev_b32_e32 v144, 2, v144
	v_lshl_add_u32 v144, v152, 12, v144
	v_lshlrev_b32_e32 v145, 3, v150
	v_lshl_add_u32 v145, v153, 2, v145
	v_lshl_add_u32 v145, v152, 12, v145
	s_waitcnt lgkmcnt(0)
	s_cmp_lt_u32 s30, 4
	s_cselect_b32 s20, s10, s24
	s_cselect_b32 s21, s11, s25
	s_add_u32 s32, s6, 0x4000
	s_addc_u32 s33, s7, 0
	s_add_u32 s34, s6, 0x8000
	s_addc_u32 s35, s7, 0
	s_add_u32 s36, s6, 0xc000
	s_addc_u32 s37, s7, 0
	s_add_u32 s38, s20, 0x4000
	s_addc_u32 s39, s21, 0
	s_add_u32 s40, s20, 0x8000
	s_addc_u32 s41, s21, 0
	s_add_u32 s42, s20, 0xc000
	s_addc_u32 s43, s21, 0
	s_mul_hi_u32 s5, s19, 0xaaaaaaab
	s_addk_i32 s16, 0xfa
	s_lshr_b32 s10, s5, 5
	s_mov_b32 s11, 0
	s_add_i32 s31, s30, s2
	s_and_b32 s31, s31, 7
	s_cmp_eq_u32 s31, 1
	s_cbranch_scc1 .Lw_rot_1
	s_cmp_eq_u32 s31, 2
	s_cbranch_scc1 .Lw_rot_2
	s_cmp_eq_u32 s31, 3
	s_cbranch_scc1 .Lw_rot_3
	s_cmp_eq_u32 s31, 4
	s_cbranch_scc1 .Lw_rot_4
	s_cmp_eq_u32 s31, 5
	s_cbranch_scc1 .Lw_rot_5
	s_cmp_eq_u32 s31, 6
	s_cbranch_scc1 .Lw_rot_6
	s_cmp_eq_u32 s31, 7
	s_cbranch_scc1 .Lw_rot_7
.Lw_rot_0:
	global_load_dword v112, v144, s[6:7]
	global_load_dwordx2 v[176:177], v145, s[20:21]
	global_load_dword v120, v144, s[32:33]
	global_load_dwordx2 v[192:193], v145, s[38:39]
	global_load_dword v128, v144, s[34:35]
	global_load_dwordx2 v[208:209], v145, s[40:41]
	global_load_dword v136, v144, s[36:37]
	global_load_dwordx2 v[224:225], v145, s[42:43]
	global_load_dword v113, v144, s[6:7] offset:512
	global_load_dwordx2 v[178:179], v145, s[20:21] offset:512
	global_load_dword v121, v144, s[32:33] offset:512
	global_load_dwordx2 v[194:195], v145, s[38:39] offset:512
	global_load_dword v129, v144, s[34:35] offset:512
	global_load_dwordx2 v[210:211], v145, s[40:41] offset:512
	global_load_dword v137, v144, s[36:37] offset:512
	global_load_dwordx2 v[226:227], v145, s[42:43] offset:512
	global_load_dword v114, v144, s[6:7] offset:1024
	global_load_dwordx2 v[180:181], v145, s[20:21] offset:1024
	global_load_dword v122, v144, s[32:33] offset:1024
	global_load_dwordx2 v[196:197], v145, s[38:39] offset:1024
	global_load_dword v130, v144, s[34:35] offset:1024
	global_load_dwordx2 v[212:213], v145, s[40:41] offset:1024
	global_load_dword v138, v144, s[36:37] offset:1024
	global_load_dwordx2 v[228:229], v145, s[42:43] offset:1024
	global_load_dword v115, v144, s[6:7] offset:1536
	global_load_dwordx2 v[182:183], v145, s[20:21] offset:1536
	global_load_dword v123, v144, s[32:33] offset:1536
	global_load_dwordx2 v[198:199], v145, s[38:39] offset:1536
	global_load_dword v131, v144, s[34:35] offset:1536
	global_load_dwordx2 v[214:215], v145, s[40:41] offset:1536
	global_load_dword v139, v144, s[36:37] offset:1536
	global_load_dwordx2 v[230:231], v145, s[42:43] offset:1536
	global_load_dword v116, v144, s[6:7] offset:2048
	global_load_dwordx2 v[184:185], v145, s[20:21] offset:2048
	global_load_dword v124, v144, s[32:33] offset:2048
	global_load_dwordx2 v[200:201], v145, s[38:39] offset:2048
	global_load_dword v132, v144, s[34:35] offset:2048
	global_load_dwordx2 v[216:217], v145, s[40:41] offset:2048
	global_load_dword v140, v144, s[36:37] offset:2048
	global_load_dwordx2 v[232:233], v145, s[42:43] offset:2048
	global_load_dword v117, v144, s[6:7] offset:2560
	global_load_dwordx2 v[186:187], v145, s[20:21] offset:2560
	global_load_dword v125, v144, s[32:33] offset:2560
	global_load_dwordx2 v[202:203], v145, s[38:39] offset:2560
	global_load_dword v133, v144, s[34:35] offset:2560
	global_load_dwordx2 v[218:219], v145, s[40:41] offset:2560
	global_load_dword v141, v144, s[36:37] offset:2560
	global_load_dwordx2 v[234:235], v145, s[42:43] offset:2560
	global_load_dword v118, v144, s[6:7] offset:3072
	global_load_dwordx2 v[188:189], v145, s[20:21] offset:3072
	global_load_dword v126, v144, s[32:33] offset:3072
	global_load_dwordx2 v[204:205], v145, s[38:39] offset:3072
	global_load_dword v134, v144, s[34:35] offset:3072
	global_load_dwordx2 v[220:221], v145, s[40:41] offset:3072
	global_load_dword v142, v144, s[36:37] offset:3072
	global_load_dwordx2 v[236:237], v145, s[42:43] offset:3072
	global_load_dword v119, v144, s[6:7] offset:3584
	global_load_dwordx2 v[190:191], v145, s[20:21] offset:3584
	global_load_dword v127, v144, s[32:33] offset:3584
	global_load_dwordx2 v[206:207], v145, s[38:39] offset:3584
	global_load_dword v135, v144, s[34:35] offset:3584
	global_load_dwordx2 v[222:223], v145, s[40:41] offset:3584
	global_load_dword v143, v144, s[36:37] offset:3584
	global_load_dwordx2 v[238:239], v145, s[42:43] offset:3584
	s_branch .Lw_ld_done
.Lw_rot_1:
	global_load_dword v113, v144, s[6:7] offset:512
	global_load_dwordx2 v[178:179], v145, s[20:21] offset:512
	global_load_dword v121, v144, s[32:33] offset:512
	global_load_dwordx2 v[194:195], v145, s[38:39] offset:512
	global_load_dword v129, v144, s[34:35] offset:512
	global_load_dwordx2 v[210:211], v145, s[40:41] offset:512
	global_load_dword v137, v144, s[36:37] offset:512
	global_load_dwordx2 v[226:227], v145, s[42:43] offset:512
	global_load_dword v114, v144, s[6:7] offset:1024
	global_load_dwordx2 v[180:181], v145, s[20:21] offset:1024
	global_load_dword v122, v144, s[32:33] offset:1024
	global_load_dwordx2 v[196:197], v145, s[38:39] offset:1024
	global_load_dword v130, v144, s[34:35] offset:1024
	global_load_dwordx2 v[212:213], v145, s[40:41] offset:1024
	global_load_dword v138, v144, s[36:37] offset:1024
	global_load_dwordx2 v[228:229], v145, s[42:43] offset:1024
	global_load_dword v115, v144, s[6:7] offset:1536
	global_load_dwordx2 v[182:183], v145, s[20:21] offset:1536
	global_load_dword v123, v144, s[32:33] offset:1536
	global_load_dwordx2 v[198:199], v145, s[38:39] offset:1536
	global_load_dword v131, v144, s[34:35] offset:1536
	global_load_dwordx2 v[214:215], v145, s[40:41] offset:1536
	global_load_dword v139, v144, s[36:37] offset:1536
	global_load_dwordx2 v[230:231], v145, s[42:43] offset:1536
	global_load_dword v116, v144, s[6:7] offset:2048
	global_load_dwordx2 v[184:185], v145, s[20:21] offset:2048
	global_load_dword v124, v144, s[32:33] offset:2048
	global_load_dwordx2 v[200:201], v145, s[38:39] offset:2048
	global_load_dword v132, v144, s[34:35] offset:2048
	global_load_dwordx2 v[216:217], v145, s[40:41] offset:2048
	global_load_dword v140, v144, s[36:37] offset:2048
	global_load_dwordx2 v[232:233], v145, s[42:43] offset:2048
	global_load_dword v117, v144, s[6:7] offset:2560
	global_load_dwordx2 v[186:187], v145, s[20:21] offset:2560
	global_load_dword v125, v144, s[32:33] offset:2560
	global_load_dwordx2 v[202:203], v145, s[38:39] offset:2560
	global_load_dword v133, v144, s[34:35] offset:2560
	global_load_dwordx2 v[218:219], v145, s[40:41] offset:2560
	global_load_dword v141, v144, s[36:37] offset:2560
	global_load_dwordx2 v[234:235], v145, s[42:43] offset:2560
	global_load_dword v118, v144, s[6:7] offset:3072
	global_load_dwordx2 v[188:189], v145, s[20:21] offset:3072
	global_load_dword v126, v144, s[32:33] offset:3072
	global_load_dwordx2 v[204:205], v145, s[38:39] offset:3072
	global_load_dword v134, v144, s[34:35] offset:3072
	global_load_dwordx2 v[220:221], v145, s[40:41] offset:3072
	global_load_dword v142, v144, s[36:37] offset:3072
	global_load_dwordx2 v[236:237], v145, s[42:43] offset:3072
	global_load_dword v119, v144, s[6:7] offset:3584
	global_load_dwordx2 v[190:191], v145, s[20:21] offset:3584
	global_load_dword v127, v144, s[32:33] offset:3584
	global_load_dwordx2 v[206:207], v145, s[38:39] offset:3584
	global_load_dword v135, v144, s[34:35] offset:3584
	global_load_dwordx2 v[222:223], v145, s[40:41] offset:3584
	global_load_dword v143, v144, s[36:37] offset:3584
	global_load_dwordx2 v[238:239], v145, s[42:43] offset:3584
	global_load_dword v112, v144, s[6:7]
	global_load_dwordx2 v[176:177], v145, s[20:21]
	global_load_dword v120, v144, s[32:33]
	global_load_dwordx2 v[192:193], v145, s[38:39]
	global_load_dword v128, v144, s[34:35]
	global_load_dwordx2 v[208:209], v145, s[40:41]
	global_load_dword v136, v144, s[36:37]
	global_load_dwordx2 v[224:225], v145, s[42:43]
	s_branch .Lw_ld_done
.Lw_rot_2:
	global_load_dword v114, v144, s[6:7] offset:1024
	global_load_dwordx2 v[180:181], v145, s[20:21] offset:1024
	global_load_dword v122, v144, s[32:33] offset:1024
	global_load_dwordx2 v[196:197], v145, s[38:39] offset:1024
	global_load_dword v130, v144, s[34:35] offset:1024
	global_load_dwordx2 v[212:213], v145, s[40:41] offset:1024
	global_load_dword v138, v144, s[36:37] offset:1024
	global_load_dwordx2 v[228:229], v145, s[42:43] offset:1024
	global_load_dword v115, v144, s[6:7] offset:1536
	global_load_dwordx2 v[182:183], v145, s[20:21] offset:1536
	global_load_dword v123, v144, s[32:33] offset:1536
	global_load_dwordx2 v[198:199], v145, s[38:39] offset:1536
	global_load_dword v131, v144, s[34:35] offset:1536
	global_load_dwordx2 v[214:215], v145, s[40:41] offset:1536
	global_load_dword v139, v144, s[36:37] offset:1536
	global_load_dwordx2 v[230:231], v145, s[42:43] offset:1536
	global_load_dword v116, v144, s[6:7] offset:2048
	global_load_dwordx2 v[184:185], v145, s[20:21] offset:2048
	global_load_dword v124, v144, s[32:33] offset:2048
	global_load_dwordx2 v[200:201], v145, s[38:39] offset:2048
	global_load_dword v132, v144, s[34:35] offset:2048
	global_load_dwordx2 v[216:217], v145, s[40:41] offset:2048
	global_load_dword v140, v144, s[36:37] offset:2048
	global_load_dwordx2 v[232:233], v145, s[42:43] offset:2048
	global_load_dword v117, v144, s[6:7] offset:2560
	global_load_dwordx2 v[186:187], v145, s[20:21] offset:2560
	global_load_dword v125, v144, s[32:33] offset:2560
	global_load_dwordx2 v[202:203], v145, s[38:39] offset:2560
	global_load_dword v133, v144, s[34:35] offset:2560
	global_load_dwordx2 v[218:219], v145, s[40:41] offset:2560
	global_load_dword v141, v144, s[36:37] offset:2560
	global_load_dwordx2 v[234:235], v145, s[42:43] offset:2560
	global_load_dword v118, v144, s[6:7] offset:3072
	global_load_dwordx2 v[188:189], v145, s[20:21] offset:3072
	global_load_dword v126, v144, s[32:33] offset:3072
	global_load_dwordx2 v[204:205], v145, s[38:39] offset:3072
	global_load_dword v134, v144, s[34:35] offset:3072
	global_load_dwordx2 v[220:221], v145, s[40:41] offset:3072
	global_load_dword v142, v144, s[36:37] offset:3072
	global_load_dwordx2 v[236:237], v145, s[42:43] offset:3072
	global_load_dword v119, v144, s[6:7] offset:3584
	global_load_dwordx2 v[190:191], v145, s[20:21] offset:3584
	global_load_dword v127, v144, s[32:33] offset:3584
	global_load_dwordx2 v[206:207], v145, s[38:39] offset:3584
	global_load_dword v135, v144, s[34:35] offset:3584
	global_load_dwordx2 v[222:223], v145, s[40:41] offset:3584
	global_load_dword v143, v144, s[36:37] offset:3584
	global_load_dwordx2 v[238:239], v145, s[42:43] offset:3584
	global_load_dword v112, v144, s[6:7]
	global_load_dwordx2 v[176:177], v145, s[20:21]
	global_load_dword v120, v144, s[32:33]
	global_load_dwordx2 v[192:193], v145, s[38:39]
	global_load_dword v128, v144, s[34:35]
	global_load_dwordx2 v[208:209], v145, s[40:41]
	global_load_dword v136, v144, s[36:37]
	global_load_dwordx2 v[224:225], v145, s[42:43]
	global_load_dword v113, v144, s[6:7] offset:512
	global_load_dwordx2 v[178:179], v145, s[20:21] offset:512
	global_load_dword v121, v144, s[32:33] offset:512
	global_load_dwordx2 v[194:195], v145, s[38:39] offset:512
	global_load_dword v129, v144, s[34:35] offset:512
	global_load_dwordx2 v[210:211], v145, s[40:41] offset:512
	global_load_dword v137, v144, s[36:37] offset:512
	global_load_dwordx2 v[226:227], v145, s[42:43] offset:512
	s_branch .Lw_ld_done
.Lw_rot_3:
	global_load_dword v115, v144, s[6:7] offset:1536
	global_load_dwordx2 v[182:183], v145, s[20:21] offset:1536
	global_load_dword v123, v144, s[32:33] offset:1536
	global_load_dwordx2 v[198:199], v145, s[38:39] offset:1536
	global_load_dword v131, v144, s[34:35] offset:1536
	global_load_dwordx2 v[214:215], v145, s[40:41] offset:1536
	global_load_dword v139, v144, s[36:37] offset:1536
	global_load_dwordx2 v[230:231], v145, s[42:43] offset:1536
	global_load_dword v116, v144, s[6:7] offset:2048
	global_load_dwordx2 v[184:185], v145, s[20:21] offset:2048
	global_load_dword v124, v144, s[32:33] offset:2048
	global_load_dwordx2 v[200:201], v145, s[38:39] offset:2048
	global_load_dword v132, v144, s[34:35] offset:2048
	global_load_dwordx2 v[216:217], v145, s[40:41] offset:2048
	global_load_dword v140, v144, s[36:37] offset:2048
	global_load_dwordx2 v[232:233], v145, s[42:43] offset:2048
	global_load_dword v117, v144, s[6:7] offset:2560
	global_load_dwordx2 v[186:187], v145, s[20:21] offset:2560
	global_load_dword v125, v144, s[32:33] offset:2560
	global_load_dwordx2 v[202:203], v145, s[38:39] offset:2560
	global_load_dword v133, v144, s[34:35] offset:2560
	global_load_dwordx2 v[218:219], v145, s[40:41] offset:2560
	global_load_dword v141, v144, s[36:37] offset:2560
	global_load_dwordx2 v[234:235], v145, s[42:43] offset:2560
	global_load_dword v118, v144, s[6:7] offset:3072
	global_load_dwordx2 v[188:189], v145, s[20:21] offset:3072
	global_load_dword v126, v144, s[32:33] offset:3072
	global_load_dwordx2 v[204:205], v145, s[38:39] offset:3072
	global_load_dword v134, v144, s[34:35] offset:3072
	global_load_dwordx2 v[220:221], v145, s[40:41] offset:3072
	global_load_dword v142, v144, s[36:37] offset:3072
	global_load_dwordx2 v[236:237], v145, s[42:43] offset:3072
	global_load_dword v119, v144, s[6:7] offset:3584
	global_load_dwordx2 v[190:191], v145, s[20:21] offset:3584
	global_load_dword v127, v144, s[32:33] offset:3584
	global_load_dwordx2 v[206:207], v145, s[38:39] offset:3584
	global_load_dword v135, v144, s[34:35] offset:3584
	global_load_dwordx2 v[222:223], v145, s[40:41] offset:3584
	global_load_dword v143, v144, s[36:37] offset:3584
	global_load_dwordx2 v[238:239], v145, s[42:43] offset:3584
	global_load_dword v112, v144, s[6:7]
	global_load_dwordx2 v[176:177], v145, s[20:21]
	global_load_dword v120, v144, s[32:33]
	global_load_dwordx2 v[192:193], v145, s[38:39]
	global_load_dword v128, v144, s[34:35]
	global_load_dwordx2 v[208:209], v145, s[40:41]
	global_load_dword v136, v144, s[36:37]
	global_load_dwordx2 v[224:225], v145, s[42:43]
	global_load_dword v113, v144, s[6:7] offset:512
	global_load_dwordx2 v[178:179], v145, s[20:21] offset:512
	global_load_dword v121, v144, s[32:33] offset:512
	global_load_dwordx2 v[194:195], v145, s[38:39] offset:512
	global_load_dword v129, v144, s[34:35] offset:512
	global_load_dwordx2 v[210:211], v145, s[40:41] offset:512
	global_load_dword v137, v144, s[36:37] offset:512
	global_load_dwordx2 v[226:227], v145, s[42:43] offset:512
	global_load_dword v114, v144, s[6:7] offset:1024
	global_load_dwordx2 v[180:181], v145, s[20:21] offset:1024
	global_load_dword v122, v144, s[32:33] offset:1024
	global_load_dwordx2 v[196:197], v145, s[38:39] offset:1024
	global_load_dword v130, v144, s[34:35] offset:1024
	global_load_dwordx2 v[212:213], v145, s[40:41] offset:1024
	global_load_dword v138, v144, s[36:37] offset:1024
	global_load_dwordx2 v[228:229], v145, s[42:43] offset:1024
	s_branch .Lw_ld_done
.Lw_rot_4:
	global_load_dword v116, v144, s[6:7] offset:2048
	global_load_dwordx2 v[184:185], v145, s[20:21] offset:2048
	global_load_dword v124, v144, s[32:33] offset:2048
	global_load_dwordx2 v[200:201], v145, s[38:39] offset:2048
	global_load_dword v132, v144, s[34:35] offset:2048
	global_load_dwordx2 v[216:217], v145, s[40:41] offset:2048
	global_load_dword v140, v144, s[36:37] offset:2048
	global_load_dwordx2 v[232:233], v145, s[42:43] offset:2048
	global_load_dword v117, v144, s[6:7] offset:2560
	global_load_dwordx2 v[186:187], v145, s[20:21] offset:2560
	global_load_dword v125, v144, s[32:33] offset:2560
	global_load_dwordx2 v[202:203], v145, s[38:39] offset:2560
	global_load_dword v133, v144, s[34:35] offset:2560
	global_load_dwordx2 v[218:219], v145, s[40:41] offset:2560
	global_load_dword v141, v144, s[36:37] offset:2560
	global_load_dwordx2 v[234:235], v145, s[42:43] offset:2560
	global_load_dword v118, v144, s[6:7] offset:3072
	global_load_dwordx2 v[188:189], v145, s[20:21] offset:3072
	global_load_dword v126, v144, s[32:33] offset:3072
	global_load_dwordx2 v[204:205], v145, s[38:39] offset:3072
	global_load_dword v134, v144, s[34:35] offset:3072
	global_load_dwordx2 v[220:221], v145, s[40:41] offset:3072
	global_load_dword v142, v144, s[36:37] offset:3072
	global_load_dwordx2 v[236:237], v145, s[42:43] offset:3072
	global_load_dword v119, v144, s[6:7] offset:3584
	global_load_dwordx2 v[190:191], v145, s[20:21] offset:3584
	global_load_dword v127, v144, s[32:33] offset:3584
	global_load_dwordx2 v[206:207], v145, s[38:39] offset:3584
	global_load_dword v135, v144, s[34:35] offset:3584
	global_load_dwordx2 v[222:223], v145, s[40:41] offset:3584
	global_load_dword v143, v144, s[36:37] offset:3584
	global_load_dwordx2 v[238:239], v145, s[42:43] offset:3584
	global_load_dword v112, v144, s[6:7]
	global_load_dwordx2 v[176:177], v145, s[20:21]
	global_load_dword v120, v144, s[32:33]
	global_load_dwordx2 v[192:193], v145, s[38:39]
	global_load_dword v128, v144, s[34:35]
	global_load_dwordx2 v[208:209], v145, s[40:41]
	global_load_dword v136, v144, s[36:37]
	global_load_dwordx2 v[224:225], v145, s[42:43]
	global_load_dword v113, v144, s[6:7] offset:512
	global_load_dwordx2 v[178:179], v145, s[20:21] offset:512
	global_load_dword v121, v144, s[32:33] offset:512
	global_load_dwordx2 v[194:195], v145, s[38:39] offset:512
	global_load_dword v129, v144, s[34:35] offset:512
	global_load_dwordx2 v[210:211], v145, s[40:41] offset:512
	global_load_dword v137, v144, s[36:37] offset:512
	global_load_dwordx2 v[226:227], v145, s[42:43] offset:512
	global_load_dword v114, v144, s[6:7] offset:1024
	global_load_dwordx2 v[180:181], v145, s[20:21] offset:1024
	global_load_dword v122, v144, s[32:33] offset:1024
	global_load_dwordx2 v[196:197], v145, s[38:39] offset:1024
	global_load_dword v130, v144, s[34:35] offset:1024
	global_load_dwordx2 v[212:213], v145, s[40:41] offset:1024
	global_load_dword v138, v144, s[36:37] offset:1024
	global_load_dwordx2 v[228:229], v145, s[42:43] offset:1024
	global_load_dword v115, v144, s[6:7] offset:1536
	global_load_dwordx2 v[182:183], v145, s[20:21] offset:1536
	global_load_dword v123, v144, s[32:33] offset:1536
	global_load_dwordx2 v[198:199], v145, s[38:39] offset:1536
	global_load_dword v131, v144, s[34:35] offset:1536
	global_load_dwordx2 v[214:215], v145, s[40:41] offset:1536
	global_load_dword v139, v144, s[36:37] offset:1536
	global_load_dwordx2 v[230:231], v145, s[42:43] offset:1536
	s_branch .Lw_ld_done
.Lw_rot_5:
	global_load_dword v117, v144, s[6:7] offset:2560
	global_load_dwordx2 v[186:187], v145, s[20:21] offset:2560
	global_load_dword v125, v144, s[32:33] offset:2560
	global_load_dwordx2 v[202:203], v145, s[38:39] offset:2560
	global_load_dword v133, v144, s[34:35] offset:2560
	global_load_dwordx2 v[218:219], v145, s[40:41] offset:2560
	global_load_dword v141, v144, s[36:37] offset:2560
	global_load_dwordx2 v[234:235], v145, s[42:43] offset:2560
	global_load_dword v118, v144, s[6:7] offset:3072
	global_load_dwordx2 v[188:189], v145, s[20:21] offset:3072
	global_load_dword v126, v144, s[32:33] offset:3072
	global_load_dwordx2 v[204:205], v145, s[38:39] offset:3072
	global_load_dword v134, v144, s[34:35] offset:3072
	global_load_dwordx2 v[220:221], v145, s[40:41] offset:3072
	global_load_dword v142, v144, s[36:37] offset:3072
	global_load_dwordx2 v[236:237], v145, s[42:43] offset:3072
	global_load_dword v119, v144, s[6:7] offset:3584
	global_load_dwordx2 v[190:191], v145, s[20:21] offset:3584
	global_load_dword v127, v144, s[32:33] offset:3584
	global_load_dwordx2 v[206:207], v145, s[38:39] offset:3584
	global_load_dword v135, v144, s[34:35] offset:3584
	global_load_dwordx2 v[222:223], v145, s[40:41] offset:3584
	global_load_dword v143, v144, s[36:37] offset:3584
	global_load_dwordx2 v[238:239], v145, s[42:43] offset:3584
	global_load_dword v112, v144, s[6:7]
	global_load_dwordx2 v[176:177], v145, s[20:21]
	global_load_dword v120, v144, s[32:33]
	global_load_dwordx2 v[192:193], v145, s[38:39]
	global_load_dword v128, v144, s[34:35]
	global_load_dwordx2 v[208:209], v145, s[40:41]
	global_load_dword v136, v144, s[36:37]
	global_load_dwordx2 v[224:225], v145, s[42:43]
	global_load_dword v113, v144, s[6:7] offset:512
	global_load_dwordx2 v[178:179], v145, s[20:21] offset:512
	global_load_dword v121, v144, s[32:33] offset:512
	global_load_dwordx2 v[194:195], v145, s[38:39] offset:512
	global_load_dword v129, v144, s[34:35] offset:512
	global_load_dwordx2 v[210:211], v145, s[40:41] offset:512
	global_load_dword v137, v144, s[36:37] offset:512
	global_load_dwordx2 v[226:227], v145, s[42:43] offset:512
	global_load_dword v114, v144, s[6:7] offset:1024
	global_load_dwordx2 v[180:181], v145, s[20:21] offset:1024
	global_load_dword v122, v144, s[32:33] offset:1024
	global_load_dwordx2 v[196:197], v145, s[38:39] offset:1024
	global_load_dword v130, v144, s[34:35] offset:1024
	global_load_dwordx2 v[212:213], v145, s[40:41] offset:1024
	global_load_dword v138, v144, s[36:37] offset:1024
	global_load_dwordx2 v[228:229], v145, s[42:43] offset:1024
	global_load_dword v115, v144, s[6:7] offset:1536
	global_load_dwordx2 v[182:183], v145, s[20:21] offset:1536
	global_load_dword v123, v144, s[32:33] offset:1536
	global_load_dwordx2 v[198:199], v145, s[38:39] offset:1536
	global_load_dword v131, v144, s[34:35] offset:1536
	global_load_dwordx2 v[214:215], v145, s[40:41] offset:1536
	global_load_dword v139, v144, s[36:37] offset:1536
	global_load_dwordx2 v[230:231], v145, s[42:43] offset:1536
	global_load_dword v116, v144, s[6:7] offset:2048
	global_load_dwordx2 v[184:185], v145, s[20:21] offset:2048
	global_load_dword v124, v144, s[32:33] offset:2048
	global_load_dwordx2 v[200:201], v145, s[38:39] offset:2048
	global_load_dword v132, v144, s[34:35] offset:2048
	global_load_dwordx2 v[216:217], v145, s[40:41] offset:2048
	global_load_dword v140, v144, s[36:37] offset:2048
	global_load_dwordx2 v[232:233], v145, s[42:43] offset:2048
	s_branch .Lw_ld_done
.Lw_rot_6:
	global_load_dword v118, v144, s[6:7] offset:3072
	global_load_dwordx2 v[188:189], v145, s[20:21] offset:3072
	global_load_dword v126, v144, s[32:33] offset:3072
	global_load_dwordx2 v[204:205], v145, s[38:39] offset:3072
	global_load_dword v134, v144, s[34:35] offset:3072
	global_load_dwordx2 v[220:221], v145, s[40:41] offset:3072
	global_load_dword v142, v144, s[36:37] offset:3072
	global_load_dwordx2 v[236:237], v145, s[42:43] offset:3072
	global_load_dword v119, v144, s[6:7] offset:3584
	global_load_dwordx2 v[190:191], v145, s[20:21] offset:3584
	global_load_dword v127, v144, s[32:33] offset:3584
	global_load_dwordx2 v[206:207], v145, s[38:39] offset:3584
	global_load_dword v135, v144, s[34:35] offset:3584
	global_load_dwordx2 v[222:223], v145, s[40:41] offset:3584
	global_load_dword v143, v144, s[36:37] offset:3584
	global_load_dwordx2 v[238:239], v145, s[42:43] offset:3584
	global_load_dword v112, v144, s[6:7]
	global_load_dwordx2 v[176:177], v145, s[20:21]
	global_load_dword v120, v144, s[32:33]
	global_load_dwordx2 v[192:193], v145, s[38:39]
	global_load_dword v128, v144, s[34:35]
	global_load_dwordx2 v[208:209], v145, s[40:41]
	global_load_dword v136, v144, s[36:37]
	global_load_dwordx2 v[224:225], v145, s[42:43]
	global_load_dword v113, v144, s[6:7] offset:512
	global_load_dwordx2 v[178:179], v145, s[20:21] offset:512
	global_load_dword v121, v144, s[32:33] offset:512
	global_load_dwordx2 v[194:195], v145, s[38:39] offset:512
	global_load_dword v129, v144, s[34:35] offset:512
	global_load_dwordx2 v[210:211], v145, s[40:41] offset:512
	global_load_dword v137, v144, s[36:37] offset:512
	global_load_dwordx2 v[226:227], v145, s[42:43] offset:512
	global_load_dword v114, v144, s[6:7] offset:1024
	global_load_dwordx2 v[180:181], v145, s[20:21] offset:1024
	global_load_dword v122, v144, s[32:33] offset:1024
	global_load_dwordx2 v[196:197], v145, s[38:39] offset:1024
	global_load_dword v130, v144, s[34:35] offset:1024
	global_load_dwordx2 v[212:213], v145, s[40:41] offset:1024
	global_load_dword v138, v144, s[36:37] offset:1024
	global_load_dwordx2 v[228:229], v145, s[42:43] offset:1024
	global_load_dword v115, v144, s[6:7] offset:1536
	global_load_dwordx2 v[182:183], v145, s[20:21] offset:1536
	global_load_dword v123, v144, s[32:33] offset:1536
	global_load_dwordx2 v[198:199], v145, s[38:39] offset:1536
	global_load_dword v131, v144, s[34:35] offset:1536
	global_load_dwordx2 v[214:215], v145, s[40:41] offset:1536
	global_load_dword v139, v144, s[36:37] offset:1536
	global_load_dwordx2 v[230:231], v145, s[42:43] offset:1536
	global_load_dword v116, v144, s[6:7] offset:2048
	global_load_dwordx2 v[184:185], v145, s[20:21] offset:2048
	global_load_dword v124, v144, s[32:33] offset:2048
	global_load_dwordx2 v[200:201], v145, s[38:39] offset:2048
	global_load_dword v132, v144, s[34:35] offset:2048
	global_load_dwordx2 v[216:217], v145, s[40:41] offset:2048
	global_load_dword v140, v144, s[36:37] offset:2048
	global_load_dwordx2 v[232:233], v145, s[42:43] offset:2048
	global_load_dword v117, v144, s[6:7] offset:2560
	global_load_dwordx2 v[186:187], v145, s[20:21] offset:2560
	global_load_dword v125, v144, s[32:33] offset:2560
	global_load_dwordx2 v[202:203], v145, s[38:39] offset:2560
	global_load_dword v133, v144, s[34:35] offset:2560
	global_load_dwordx2 v[218:219], v145, s[40:41] offset:2560
	global_load_dword v141, v144, s[36:37] offset:2560
	global_load_dwordx2 v[234:235], v145, s[42:43] offset:2560
	s_branch .Lw_ld_done
.Lw_rot_7:
	global_load_dword v119, v144, s[6:7] offset:3584
	global_load_dwordx2 v[190:191], v145, s[20:21] offset:3584
	global_load_dword v127, v144, s[32:33] offset:3584
	global_load_dwordx2 v[206:207], v145, s[38:39] offset:3584
	global_load_dword v135, v144, s[34:35] offset:3584
	global_load_dwordx2 v[222:223], v145, s[40:41] offset:3584
	global_load_dword v143, v144, s[36:37] offset:3584
	global_load_dwordx2 v[238:239], v145, s[42:43] offset:3584
	global_load_dword v112, v144, s[6:7]
	global_load_dwordx2 v[176:177], v145, s[20:21]
	global_load_dword v120, v144, s[32:33]
	global_load_dwordx2 v[192:193], v145, s[38:39]
	global_load_dword v128, v144, s[34:35]
	global_load_dwordx2 v[208:209], v145, s[40:41]
	global_load_dword v136, v144, s[36:37]
	global_load_dwordx2 v[224:225], v145, s[42:43]
	global_load_dword v113, v144, s[6:7] offset:512
	global_load_dwordx2 v[178:179], v145, s[20:21] offset:512
	global_load_dword v121, v144, s[32:33] offset:512
	global_load_dwordx2 v[194:195], v145, s[38:39] offset:512
	global_load_dword v129, v144, s[34:35] offset:512
	global_load_dwordx2 v[210:211], v145, s[40:41] offset:512
	global_load_dword v137, v144, s[36:37] offset:512
	global_load_dwordx2 v[226:227], v145, s[42:43] offset:512
	global_load_dword v114, v144, s[6:7] offset:1024
	global_load_dwordx2 v[180:181], v145, s[20:21] offset:1024
	global_load_dword v122, v144, s[32:33] offset:1024
	global_load_dwordx2 v[196:197], v145, s[38:39] offset:1024
	global_load_dword v130, v144, s[34:35] offset:1024
	global_load_dwordx2 v[212:213], v145, s[40:41] offset:1024
	global_load_dword v138, v144, s[36:37] offset:1024
	global_load_dwordx2 v[228:229], v145, s[42:43] offset:1024
	global_load_dword v115, v144, s[6:7] offset:1536
	global_load_dwordx2 v[182:183], v145, s[20:21] offset:1536
	global_load_dword v123, v144, s[32:33] offset:1536
	global_load_dwordx2 v[198:199], v145, s[38:39] offset:1536
	global_load_dword v131, v144, s[34:35] offset:1536
	global_load_dwordx2 v[214:215], v145, s[40:41] offset:1536
	global_load_dword v139, v144, s[36:37] offset:1536
	global_load_dwordx2 v[230:231], v145, s[42:43] offset:1536
	global_load_dword v116, v144, s[6:7] offset:2048
	global_load_dwordx2 v[184:185], v145, s[20:21] offset:2048
	global_load_dword v124, v144, s[32:33] offset:2048
	global_load_dwordx2 v[200:201], v145, s[38:39] offset:2048
	global_load_dword v132, v144, s[34:35] offset:2048
	global_load_dwordx2 v[216:217], v145, s[40:41] offset:2048
	global_load_dword v140, v144, s[36:37] offset:2048
	global_load_dwordx2 v[232:233], v145, s[42:43] offset:2048
	global_load_dword v117, v144, s[6:7] offset:2560
	global_load_dwordx2 v[186:187], v145, s[20:21] offset:2560
	global_load_dword v125, v144, s[32:33] offset:2560
	global_load_dwordx2 v[202:203], v145, s[38:39] offset:2560
	global_load_dword v133, v144, s[34:35] offset:2560
	global_load_dwordx2 v[218:219], v145, s[40:41] offset:2560
	global_load_dword v141, v144, s[36:37] offset:2560
	global_load_dwordx2 v[234:235], v145, s[42:43] offset:2560
	global_load_dword v118, v144, s[6:7] offset:3072
	global_load_dwordx2 v[188:189], v145, s[20:21] offset:3072
	global_load_dword v126, v144, s[32:33] offset:3072
	global_load_dwordx2 v[204:205], v145, s[38:39] offset:3072
	global_load_dword v134, v144, s[34:35] offset:3072
	global_load_dwordx2 v[220:221], v145, s[40:41] offset:3072
	global_load_dword v142, v144, s[36:37] offset:3072
	global_load_dwordx2 v[236:237], v145, s[42:43] offset:3072
.Lw_ld_done:
	s_waitcnt vmcnt(60)
	v_and_b32_e32 v242, 0xffff0000, v3
	v_lshlrev_b32_e32 v240, 3, v0
	v_sub_f32_e32 v244, v3, v242
	v_and_b32_e32 v242, 0xffff0000, v4
	v_and_b32_e32 v148, 0xf8, v240
	v_and_b32_e32 v240, 0xffff0000, v2
	v_sub_f32_e32 v245, v4, v242
	v_and_b32_e32 v242, 0xffff0000, v5
	v_sub_f32_e32 v240, v2, v240
	v_sub_f32_e32 v246, v5, v242
	v_mad_u32_u24 v247, v1, s17, v148
	v_perm_b32 v242, v3, v2, s14
	v_perm_b32 v243, v5, v4, s14
	ds_write_b64 v247, v[242:243]
	v_perm_b32 v242, v244, v240, s14
	v_perm_b32 v243, v246, v245, s14
	ds_write_b64 v247, v[242:243] offset:13056
	v_and_b32_e32 v242, 0xffff0000, v7
	v_sub_f32_e32 v244, v7, v242
	v_and_b32_e32 v242, 0xffff0000, v8
	v_and_b32_e32 v240, 0xffff0000, v6
	v_sub_f32_e32 v245, v8, v242
	v_and_b32_e32 v242, 0xffff0000, v9
	v_sub_f32_e32 v240, v6, v240
	v_sub_f32_e32 v246, v9, v242
	v_mad_u32_u24 v241, v146, s17, v148
	v_perm_b32 v242, v7, v6, s14
	v_perm_b32 v243, v9, v8, s14
	ds_write_b64 v241, v[242:243]
	v_perm_b32 v242, v244, v240, s14
	v_perm_b32 v243, v246, v245, s14
	ds_write_b64 v241, v[242:243] offset:13056
	v_and_b32_e32 v242, 0xffff0000, v11
	v_sub_f32_e32 v244, v11, v242
	v_and_b32_e32 v242, 0xffff0000, v12
	v_and_b32_e32 v240, 0xffff0000, v10
	v_sub_f32_e32 v245, v12, v242
	v_and_b32_e32 v242, 0xffff0000, v13
	v_sub_f32_e32 v240, v10, v240
	v_sub_f32_e32 v246, v13, v242
	v_perm_b32 v242, v11, v10, s14
	v_perm_b32 v243, v13, v12, s14
	ds_write_b64 v247, v[242:243] offset:8704
	v_perm_b32 v242, v244, v240, s14
	v_perm_b32 v243, v246, v245, s14
	ds_write_b64 v247, v[242:243] offset:21760
	s_waitcnt lgkmcnt(0)
	s_barrier
	s_waitcnt vmcnt(0)
	v_cvt_pk_bf16_f32 v106, v112, v113
	v_lshlrev_b32_e32 v248, 16, v106
	v_and_b32_e32 v249, 0xffff0000, v106
	v_sub_f32_e32 v248, v112, v248
	v_sub_f32_e32 v249, v113, v249
	v_cvt_pk_bf16_f32 v102, v248, v249
	v_cvt_pk_bf16_f32 v107, v114, v115
	v_lshlrev_b32_e32 v250, 16, v107
	v_and_b32_e32 v251, 0xffff0000, v107
	v_sub_f32_e32 v250, v114, v250
	v_sub_f32_e32 v251, v115, v251
	v_cvt_pk_bf16_f32 v103, v250, v251
	v_cvt_pk_bf16_f32 v108, v116, v117
	v_lshlrev_b32_e32 v248, 16, v108
	v_and_b32_e32 v249, 0xffff0000, v108
	v_sub_f32_e32 v248, v116, v248
	v_sub_f32_e32 v249, v117, v249
	v_cvt_pk_bf16_f32 v104, v248, v249
	v_cvt_pk_bf16_f32 v109, v118, v119
	v_lshlrev_b32_e32 v250, 16, v109
	v_and_b32_e32 v251, 0xffff0000, v109
	v_sub_f32_e32 v250, v118, v250
	v_sub_f32_e32 v251, v119, v251
	v_cvt_pk_bf16_f32 v105, v250, v251
	v_cvt_pk_bf16_f32 v74, v176, v178
	v_lshlrev_b32_e32 v248, 16, v74
	v_and_b32_e32 v249, 0xffff0000, v74
	v_sub_f32_e32 v248, v176, v248
	v_sub_f32_e32 v249, v178, v249
	v_cvt_pk_bf16_f32 v70, v248, v249
	v_cvt_pk_bf16_f32 v75, v180, v182
	v_lshlrev_b32_e32 v250, 16, v75
	v_and_b32_e32 v251, 0xffff0000, v75
	v_sub_f32_e32 v250, v180, v250
	v_sub_f32_e32 v251, v182, v251
	v_cvt_pk_bf16_f32 v71, v250, v251
	v_cvt_pk_bf16_f32 v76, v184, v186
	v_lshlrev_b32_e32 v248, 16, v76
	v_and_b32_e32 v249, 0xffff0000, v76
	v_sub_f32_e32 v248, v184, v248
	v_sub_f32_e32 v249, v186, v249
	v_cvt_pk_bf16_f32 v72, v248, v249
	v_cvt_pk_bf16_f32 v77, v188, v190
	v_lshlrev_b32_e32 v250, 16, v77
	v_and_b32_e32 v251, 0xffff0000, v77
	v_sub_f32_e32 v250, v188, v250
	v_sub_f32_e32 v251, v190, v251
	v_cvt_pk_bf16_f32 v73, v250, v251
	v_cvt_pk_bf16_f32 v38, v177, v179
	v_lshlrev_b32_e32 v248, 16, v38
	v_and_b32_e32 v249, 0xffff0000, v38
	v_sub_f32_e32 v248, v177, v248
	v_sub_f32_e32 v249, v179, v249
	v_cvt_pk_bf16_f32 v42, v248, v249
	v_cvt_pk_bf16_f32 v39, v181, v183
	v_lshlrev_b32_e32 v250, 16, v39
	v_and_b32_e32 v251, 0xffff0000, v39
	v_sub_f32_e32 v250, v181, v250
	v_sub_f32_e32 v251, v183, v251
	v_cvt_pk_bf16_f32 v43, v250, v251
	v_cvt_pk_bf16_f32 v40, v185, v187
	v_lshlrev_b32_e32 v248, 16, v40
	v_and_b32_e32 v249, 0xffff0000, v40
	v_sub_f32_e32 v248, v185, v248
	v_sub_f32_e32 v249, v187, v249
	v_cvt_pk_bf16_f32 v44, v248, v249
	v_cvt_pk_bf16_f32 v41, v189, v191
	v_lshlrev_b32_e32 v250, 16, v41
	v_and_b32_e32 v251, 0xffff0000, v41
	v_sub_f32_e32 v250, v189, v250
	v_sub_f32_e32 v251, v191, v251
	v_cvt_pk_bf16_f32 v45, v250, v251
	v_cvt_pk_bf16_f32 v98, v120, v121
	v_lshlrev_b32_e32 v248, 16, v98
	v_and_b32_e32 v249, 0xffff0000, v98
	v_sub_f32_e32 v248, v120, v248
	v_sub_f32_e32 v249, v121, v249
	v_cvt_pk_bf16_f32 v94, v248, v249
	v_cvt_pk_bf16_f32 v99, v122, v123
	v_lshlrev_b32_e32 v250, 16, v99
	v_and_b32_e32 v251, 0xffff0000, v99
	v_sub_f32_e32 v250, v122, v250
	v_sub_f32_e32 v251, v123, v251
	v_cvt_pk_bf16_f32 v95, v250, v251
	v_cvt_pk_bf16_f32 v100, v124, v125
	v_lshlrev_b32_e32 v248, 16, v100
	v_and_b32_e32 v249, 0xffff0000, v100
	v_sub_f32_e32 v248, v124, v248
	v_sub_f32_e32 v249, v125, v249
	v_cvt_pk_bf16_f32 v96, v248, v249
	v_cvt_pk_bf16_f32 v101, v126, v127
	v_lshlrev_b32_e32 v250, 16, v101
	v_and_b32_e32 v251, 0xffff0000, v101
	v_sub_f32_e32 v250, v126, v250
	v_sub_f32_e32 v251, v127, v251
	v_cvt_pk_bf16_f32 v97, v250, v251
	v_cvt_pk_bf16_f32 v62, v192, v194
	v_lshlrev_b32_e32 v248, 16, v62
	v_and_b32_e32 v249, 0xffff0000, v62
	v_sub_f32_e32 v248, v192, v248
	v_sub_f32_e32 v249, v194, v249
	v_cvt_pk_bf16_f32 v66, v248, v249
	v_cvt_pk_bf16_f32 v63, v196, v198
	v_lshlrev_b32_e32 v250, 16, v63
	v_and_b32_e32 v251, 0xffff0000, v63
	v_sub_f32_e32 v250, v196, v250
	v_sub_f32_e32 v251, v198, v251
	v_cvt_pk_bf16_f32 v67, v250, v251
	v_cvt_pk_bf16_f32 v64, v200, v202
	v_lshlrev_b32_e32 v248, 16, v64
	v_and_b32_e32 v249, 0xffff0000, v64
	v_sub_f32_e32 v248, v200, v248
	v_sub_f32_e32 v249, v202, v249
	v_cvt_pk_bf16_f32 v68, v248, v249
	v_cvt_pk_bf16_f32 v65, v204, v206
	v_lshlrev_b32_e32 v250, 16, v65
	v_and_b32_e32 v251, 0xffff0000, v65
	v_sub_f32_e32 v250, v204, v250
	v_sub_f32_e32 v251, v206, v251
	v_cvt_pk_bf16_f32 v69, v250, v251
	v_cvt_pk_bf16_f32 v30, v193, v195
	v_lshlrev_b32_e32 v248, 16, v30
	v_and_b32_e32 v249, 0xffff0000, v30
	v_sub_f32_e32 v248, v193, v248
	v_sub_f32_e32 v249, v195, v249
	v_cvt_pk_bf16_f32 v34, v248, v249
	v_cvt_pk_bf16_f32 v31, v197, v199
	v_lshlrev_b32_e32 v250, 16, v31
	v_and_b32_e32 v251, 0xffff0000, v31
	v_sub_f32_e32 v250, v197, v250
	v_sub_f32_e32 v251, v199, v251
	v_cvt_pk_bf16_f32 v35, v250, v251
	v_cvt_pk_bf16_f32 v32, v201, v203
	v_lshlrev_b32_e32 v248, 16, v32
	v_and_b32_e32 v249, 0xffff0000, v32
	v_sub_f32_e32 v248, v201, v248
	v_sub_f32_e32 v249, v203, v249
	v_cvt_pk_bf16_f32 v36, v248, v249
	v_cvt_pk_bf16_f32 v33, v205, v207
	v_lshlrev_b32_e32 v250, 16, v33
	v_and_b32_e32 v251, 0xffff0000, v33
	v_sub_f32_e32 v250, v205, v250
	v_sub_f32_e32 v251, v207, v251
	v_cvt_pk_bf16_f32 v37, v250, v251
	v_cvt_pk_bf16_f32 v90, v128, v129
	v_lshlrev_b32_e32 v248, 16, v90
	v_and_b32_e32 v249, 0xffff0000, v90
	v_sub_f32_e32 v248, v128, v248
	v_sub_f32_e32 v249, v129, v249
	v_cvt_pk_bf16_f32 v86, v248, v249
	v_cvt_pk_bf16_f32 v91, v130, v131
	v_lshlrev_b32_e32 v250, 16, v91
	v_and_b32_e32 v251, 0xffff0000, v91
	v_sub_f32_e32 v250, v130, v250
	v_sub_f32_e32 v251, v131, v251
	v_cvt_pk_bf16_f32 v87, v250, v251
	v_cvt_pk_bf16_f32 v92, v132, v133
	v_lshlrev_b32_e32 v248, 16, v92
	v_and_b32_e32 v249, 0xffff0000, v92
	v_sub_f32_e32 v248, v132, v248
	v_sub_f32_e32 v249, v133, v249
	v_cvt_pk_bf16_f32 v88, v248, v249
	v_cvt_pk_bf16_f32 v93, v134, v135
	v_lshlrev_b32_e32 v250, 16, v93
	v_and_b32_e32 v251, 0xffff0000, v93
	v_sub_f32_e32 v250, v134, v250
	v_sub_f32_e32 v251, v135, v251
	v_cvt_pk_bf16_f32 v89, v250, v251
	v_cvt_pk_bf16_f32 v54, v208, v210
	v_lshlrev_b32_e32 v248, 16, v54
	v_and_b32_e32 v249, 0xffff0000, v54
	v_sub_f32_e32 v248, v208, v248
	v_sub_f32_e32 v249, v210, v249
	v_cvt_pk_bf16_f32 v58, v248, v249
	v_cvt_pk_bf16_f32 v55, v212, v214
	v_lshlrev_b32_e32 v250, 16, v55
	v_and_b32_e32 v251, 0xffff0000, v55
	v_sub_f32_e32 v250, v212, v250
	v_sub_f32_e32 v251, v214, v251
	v_cvt_pk_bf16_f32 v59, v250, v251
	v_cvt_pk_bf16_f32 v56, v216, v218
	v_lshlrev_b32_e32 v248, 16, v56
	v_and_b32_e32 v249, 0xffff0000, v56
	v_sub_f32_e32 v248, v216, v248
	v_sub_f32_e32 v249, v218, v249
	v_cvt_pk_bf16_f32 v60, v248, v249
	v_cvt_pk_bf16_f32 v57, v220, v222
	v_lshlrev_b32_e32 v250, 16, v57
	v_and_b32_e32 v251, 0xffff0000, v57
	v_sub_f32_e32 v250, v220, v250
	v_sub_f32_e32 v251, v222, v251
	v_cvt_pk_bf16_f32 v61, v250, v251
	v_cvt_pk_bf16_f32 v26, v209, v211
	v_lshlrev_b32_e32 v248, 16, v26
	v_and_b32_e32 v249, 0xffff0000, v26
	v_sub_f32_e32 v248, v209, v248
	v_sub_f32_e32 v249, v211, v249
	v_cvt_pk_bf16_f32 v22, v248, v249
	v_cvt_pk_bf16_f32 v27, v213, v215
	v_lshlrev_b32_e32 v250, 16, v27
	v_and_b32_e32 v251, 0xffff0000, v27
	v_sub_f32_e32 v250, v213, v250
	v_sub_f32_e32 v251, v215, v251
	v_cvt_pk_bf16_f32 v23, v250, v251
	v_cvt_pk_bf16_f32 v28, v217, v219
	v_lshlrev_b32_e32 v248, 16, v28
	v_and_b32_e32 v249, 0xffff0000, v28
	v_sub_f32_e32 v248, v217, v248
	v_sub_f32_e32 v249, v219, v249
	v_cvt_pk_bf16_f32 v24, v248, v249
	v_cvt_pk_bf16_f32 v29, v221, v223
	v_lshlrev_b32_e32 v250, 16, v29
	v_and_b32_e32 v251, 0xffff0000, v29
	v_sub_f32_e32 v250, v221, v250
	v_sub_f32_e32 v251, v223, v251
	v_cvt_pk_bf16_f32 v25, v250, v251
	v_cvt_pk_bf16_f32 v82, v136, v137
	v_lshlrev_b32_e32 v248, 16, v82
	v_and_b32_e32 v249, 0xffff0000, v82
	v_sub_f32_e32 v248, v136, v248
	v_sub_f32_e32 v249, v137, v249
	v_cvt_pk_bf16_f32 v78, v248, v249
	v_cvt_pk_bf16_f32 v83, v138, v139
	v_lshlrev_b32_e32 v250, 16, v83
	v_and_b32_e32 v251, 0xffff0000, v83
	v_sub_f32_e32 v250, v138, v250
	v_sub_f32_e32 v251, v139, v251
	v_cvt_pk_bf16_f32 v79, v250, v251
	v_cvt_pk_bf16_f32 v84, v140, v141
	v_lshlrev_b32_e32 v248, 16, v84
	v_and_b32_e32 v249, 0xffff0000, v84
	v_sub_f32_e32 v248, v140, v248
	v_sub_f32_e32 v249, v141, v249
	v_cvt_pk_bf16_f32 v80, v248, v249
	v_cvt_pk_bf16_f32 v85, v142, v143
	v_lshlrev_b32_e32 v250, 16, v85
	v_and_b32_e32 v251, 0xffff0000, v85
	v_sub_f32_e32 v250, v142, v250
	v_sub_f32_e32 v251, v143, v251
	v_cvt_pk_bf16_f32 v81, v250, v251
	v_cvt_pk_bf16_f32 v46, v224, v226
	v_lshlrev_b32_e32 v248, 16, v46
	v_and_b32_e32 v249, 0xffff0000, v46
	v_sub_f32_e32 v248, v224, v248
	v_sub_f32_e32 v249, v226, v249
	v_cvt_pk_bf16_f32 v50, v248, v249
	v_cvt_pk_bf16_f32 v47, v228, v230
	v_lshlrev_b32_e32 v250, 16, v47
	v_and_b32_e32 v251, 0xffff0000, v47
	v_sub_f32_e32 v250, v228, v250
	v_sub_f32_e32 v251, v230, v251
	v_cvt_pk_bf16_f32 v51, v250, v251
	v_cvt_pk_bf16_f32 v48, v232, v234
	v_lshlrev_b32_e32 v248, 16, v48
	v_and_b32_e32 v249, 0xffff0000, v48
	v_sub_f32_e32 v248, v232, v248
	v_sub_f32_e32 v249, v234, v249
	v_cvt_pk_bf16_f32 v52, v248, v249
	v_cvt_pk_bf16_f32 v49, v236, v238
	v_lshlrev_b32_e32 v250, 16, v49
	v_and_b32_e32 v251, 0xffff0000, v49
	v_sub_f32_e32 v250, v236, v250
	v_sub_f32_e32 v251, v238, v251
	v_cvt_pk_bf16_f32 v53, v250, v251
	v_cvt_pk_bf16_f32 v18, v225, v227
	v_lshlrev_b32_e32 v248, 16, v18
	v_and_b32_e32 v249, 0xffff0000, v18
	v_sub_f32_e32 v248, v225, v248
	v_sub_f32_e32 v249, v227, v249
	v_cvt_pk_bf16_f32 v14, v248, v249
	v_cvt_pk_bf16_f32 v19, v229, v231
	v_lshlrev_b32_e32 v250, 16, v19
	v_and_b32_e32 v251, 0xffff0000, v19
	v_sub_f32_e32 v250, v229, v250
	v_sub_f32_e32 v251, v231, v251
	v_cvt_pk_bf16_f32 v15, v250, v251
	v_cvt_pk_bf16_f32 v20, v233, v235
	v_lshlrev_b32_e32 v248, 16, v20
	v_and_b32_e32 v249, 0xffff0000, v20
	v_sub_f32_e32 v248, v233, v248
	v_sub_f32_e32 v249, v235, v249
	v_cvt_pk_bf16_f32 v16, v248, v249
	v_cvt_pk_bf16_f32 v21, v237, v239
	v_lshlrev_b32_e32 v250, 16, v21
	v_and_b32_e32 v251, 0xffff0000, v21
	v_sub_f32_e32 v250, v237, v250
	v_sub_f32_e32 v251, v239, v251
	v_cvt_pk_bf16_f32 v17, v250, v251
	v_mov_b32_e32 v113, 0
	v_cmp_gt_u32_e32 vcc, 0x100, v0
	v_and_b32_e32 v115, 63, v0
	v_lshrrev_b32_e32 v125, 2, v115
	v_lshlrev_b32_e32 v114, 2, v0
	v_and_b32_e32 v114, 12, v114
	v_mul_u32_u24_e32 v115, 20, v125
	v_mul_u32_u24_e32 v112, 0xa00, v149
	v_lshlrev_b32_e32 v115, 2, v115
	v_lshlrev_b32_e32 v120, 2, v114
	v_add3_u32 v118, v112, v115, v120
	v_lshlrev_b32_e32 v112, 2, v151
	v_lshl_add_u64 v[114:115], s[26:27], 0, v[112:113]
	v_mov_b32_e32 v112, 0x100
	v_cndmask_b32_e64 v112, v112, 0, vcc
	v_lshl_add_u64 v[122:123], s[28:29], 0, v[112:113]
	v_lshlrev_b32_e32 v112, 1, v153
	v_mov_b32_e32 v121, v113
	v_lshl_add_u64 v[112:113], v[122:123], 0, v[112:113]
	v_lshl_add_u64 v[114:115], v[114:115], 0, v[120:121]
	v_lshl_add_u64 v[112:113], v[112:113], 0, v[120:121]
	v_mul_u32_u24_e32 v120, 0x50, v152
	v_or_b32_e32 v120, v120, v150
	v_and_b32_e32 v124, 48, v0
	s_movk_i32 s4, 0xa00
	v_lshlrev_b32_e32 v120, 2, v120
	v_add_u32_e32 v122, s15, v125
	v_mul_u32_u24_e32 v116, 0x110, v1
	v_mul_u32_u24_e32 v117, 0x110, v146
	v_or_b32_e32 v119, 0xc350, v125
	s_max_u32 s6, s10, 1
	v_mad_u32_u24 v120, v149, s4, v120
	v_mad_u32_u24 v121, v150, s17, v124
	v_add_u32_e32 v122, 0xffffd887, v122
	v_add_u32_e32 v240, 0xcc00, v120
	v_add_u32_e32 v241, 0xd000, v120
	v_mov_b32_e32 v242, v119
	v_mov_b32_e32 v243, 0
	v_lshlrev_b64 v[244:245], 9, v[242:243]
	v_lshl_add_u64 v[228:229], v[114:115], 0, v[244:245]
	v_lshl_add_u64 v[230:231], v[112:113], 0, v[244:245]
	s_branch .LBB0_9
